# DSA steady loop: row-sum adds and bf16 packs moved out of the QK^T MFMA gaps to after the last QK^T MFMA (experiment on top of table mask + trims)
# baseline (speedup 1.0000x reference)
.LBB0_1077:
	v_lshl_add_u64 v[14:15], v[184:185], 0, s[54:55]
	s_mov_b32 s38, 0xeb20000
	v_add_co_u32_e32 v2, vcc, s38, v14
	s_mov_b32 s38, 0xeb28000
	s_nop 0
	v_addc_co_u32_e32 v3, vcc, 0, v15, vcc
	v_add_co_u32_e32 v4, vcc, s38, v14
	v_add_u32_e32 v12, s29, v239
	s_nop 0
	v_addc_co_u32_e32 v5, vcc, 0, v15, vcc
	global_load_dword v0, v[2:3], off
	global_load_dword v190, v[4:5], off
	global_load_dword v191, v[182:183], off offset:-4
	v_lshrrev_b32_e32 v2, v238, v211
	v_lshrrev_b32_e32 v3, v238, v213
	v_bfe_u32 v4, v2, 0, 4
	v_lshl_add_u32 v4, v4, 4, s100
	ds_read_b128 v[80:83], v4
	v_bfe_u32 v4, v2, 8, 4
	v_lshl_add_u32 v4, v4, 4, s100
	ds_read_b128 v[84:87], v4
	v_bfe_u32 v4, v2, 16, 4
	v_lshl_add_u32 v4, v4, 4, s100
	ds_read_b128 v[88:91], v4
	v_bfe_u32 v4, v2, 24, 4
	v_lshl_add_u32 v4, v4, 4, s100
	ds_read_b128 v[92:95], v4
	v_bfe_u32 v4, v3, 0, 4
	v_lshl_add_u32 v4, v4, 4, s100
	ds_read_b128 v[96:99], v4
	v_bfe_u32 v4, v3, 8, 4
	v_lshl_add_u32 v4, v4, 4, s100
	ds_read_b128 v[100:103], v4
	v_bfe_u32 v4, v3, 16, 4
	v_lshl_add_u32 v4, v4, 4, s100
	ds_read_b128 v[104:107], v4
	v_bfe_u32 v4, v3, 24, 4
	v_lshl_add_u32 v4, v4, 4, s100
	ds_read_b128 v[108:111], v4
	ds_read_b64_tr_b16 v[176:177], v12 offset:24576
	ds_read_b64_tr_b16 v[178:179], v12 offset:25088
	s_waitcnt lgkmcnt(6)
	v_mfma_f32_32x32x16_bf16 v[80:95], v[172:175], v[124:127], v[80:95]
	ds_read_b64_tr_b16 v[172:173], v12 offset:28672
	ds_read_b64_tr_b16 v[174:175], v12 offset:29184
	s_waitcnt lgkmcnt(4)
	v_mfma_f32_32x32x16_bf16 v[96:111], v[164:167], v[124:127], v[96:111]
	ds_read_b64_tr_b16 v[164:165], v12 offset:25600
	ds_read_b64_tr_b16 v[166:167], v12 offset:26112
	s_waitcnt lgkmcnt(11)
	v_mfma_f32_32x32x16_bf16 v[80:95], v[168:171], v[120:123], v[80:95]
	ds_read_b64_tr_b16 v[168:169], v12 offset:29696
	ds_read_b64_tr_b16 v[170:171], v12 offset:30208
	s_waitcnt lgkmcnt(12)
	v_mfma_f32_32x32x16_bf16 v[96:111], v[160:163], v[120:123], v[96:111]
	ds_read_b64_tr_b16 v[160:161], v12 offset:26624
	ds_read_b64_tr_b16 v[162:163], v12 offset:27136
	s_waitcnt lgkmcnt(13)
	v_mfma_f32_32x32x16_bf16 v[80:95], v[156:159], v[116:119], v[80:95]
	ds_read_b64_tr_b16 v[2:3], v12 offset:30720
	ds_read_b64_tr_b16 v[4:5], v12 offset:31232
	s_waitcnt lgkmcnt(14)
	v_mfma_f32_32x32x16_bf16 v[96:111], v[152:155], v[116:119], v[96:111]
	ds_read_b64_tr_b16 v[6:7], v12 offset:27648
	ds_read_b64_tr_b16 v[8:9], v12 offset:28160
	s_waitcnt lgkmcnt(14)
	v_mfma_f32_32x32x16_bf16 v[80:95], v[148:151], v[112:115], v[80:95]
	ds_read_b64_tr_b16 v[10:11], v12 offset:31744
	ds_read_b64_tr_b16 v[12:13], v12 offset:32256
	v_mfma_f32_32x32x16_bf16 v[96:111], v[144:147], v[112:115], v[96:111]
	v_add_f32_e32 v229, v64, v65
	v_add_f32_e32 v229, v66, v229
	v_add_f32_e32 v229, v67, v229
	v_add_f32_e32 v229, v68, v229
	v_add_f32_e32 v229, v69, v229
	v_add_f32_e32 v229, v70, v229
	v_add_f32_e32 v229, v71, v229
	v_add_f32_e32 v229, v72, v229
	v_add_f32_e32 v229, v73, v229
	v_add_f32_e32 v229, v74, v229
	v_add_f32_e32 v229, v75, v229
	v_add_f32_e32 v229, v76, v229
	v_add_f32_e32 v229, v77, v229
	v_add_f32_e32 v229, v78, v229
	v_add_f32_e32 v229, v79, v229
	v_add_f32_e32 v229, v48, v229
	v_add_f32_e32 v229, v49, v229
	v_add_f32_e32 v229, v50, v229
	v_add_f32_e32 v229, v51, v229
	v_add_f32_e32 v229, v52, v229
	v_add_f32_e32 v229, v53, v229
	v_add_f32_e32 v229, v54, v229
	v_add_f32_e32 v229, v55, v229
	v_add_f32_e32 v229, v56, v229
	v_add_f32_e32 v229, v57, v229
	v_add_f32_e32 v229, v58, v229
	v_add_f32_e32 v229, v59, v229
	v_add_f32_e32 v229, v60, v229
	v_add_f32_e32 v229, v61, v229
	v_add_f32_e32 v229, v62, v229
	v_add_f32_e32 v229, v63, v229
	v_cvt_pk_bf16_f32 v140, v64, v65
	v_cvt_pk_bf16_f32 v141, v66, v67
	v_cvt_pk_bf16_f32 v142, v68, v69
	v_cvt_pk_bf16_f32 v143, v70, v71
	v_cvt_pk_bf16_f32 v136, v72, v73
	v_cvt_pk_bf16_f32 v137, v74, v75
	v_cvt_pk_bf16_f32 v138, v76, v77
	v_cvt_pk_bf16_f32 v139, v78, v79
	v_cvt_pk_bf16_f32 v132, v48, v49
	v_cvt_pk_bf16_f32 v133, v50, v51
	v_cvt_pk_bf16_f32 v134, v52, v53
	v_cvt_pk_bf16_f32 v135, v54, v55
	v_cvt_pk_bf16_f32 v128, v56, v57
	v_cvt_pk_bf16_f32 v129, v58, v59
	v_cvt_pk_bf16_f32 v130, v60, v61
	v_cvt_pk_bf16_f32 v131, v62, v63
	v_lshl_add_u64 v[186:187], v[216:217], 0, s[54:55]
	v_lshl_add_u64 v[50:51], v[186:187], 0, s[20:21]
	s_add_i32 s29, s59, s63
	s_mov_b32 m0, s29
	s_nop 0
	global_load_lds_dwordx4 v[50:51], off
	v_lshl_add_u64 v[188:189], v[218:219], 0, s[54:55]
	v_lshl_add_u64 v[50:51], v[188:189], 0, s[24:25]
	s_add_i32 s29, s57, s62
	s_mov_b32 m0, s29
	s_nop 0
	global_load_lds_dwordx4 v[50:51], off
	s_waitcnt vmcnt(7)
	v_mul_f32_e32 v49, v201, v209
	v_cmp_nge_f32_e32 vcc, s73, v49
	v_cmp_neq_f32_e64 s[38:39], 0, v207
	s_or_b64 vcc, vcc, s[38:39]
	s_cmp_lg_u64 vcc, 0
	s_cselect_b64 s[38:39], -1, 0
	s_cbranch_vccz .LBB0_1079
	v_sub_f32_e32 v95, v95, v207
	v_sub_f32_e32 v94, v94, v207
	v_sub_f32_e32 v93, v93, v207
	v_sub_f32_e32 v92, v92, v207
	v_sub_f32_e32 v91, v91, v207
	v_sub_f32_e32 v90, v90, v207
	v_sub_f32_e32 v89, v89, v207
	v_sub_f32_e32 v88, v88, v207
	v_sub_f32_e32 v87, v87, v207
	v_sub_f32_e32 v86, v86, v207
	v_sub_f32_e32 v85, v85, v207
	v_sub_f32_e32 v84, v84, v207
	v_sub_f32_e32 v83, v83, v207
	v_sub_f32_e32 v82, v82, v207
	v_sub_f32_e32 v81, v81, v207
	v_sub_f32_e32 v80, v80, v207
	v_sub_f32_e32 v111, v111, v207
	v_sub_f32_e32 v110, v110, v207
	v_sub_f32_e32 v109, v109, v207
	v_sub_f32_e32 v108, v108, v207
	v_sub_f32_e32 v107, v107, v207
	v_sub_f32_e32 v106, v106, v207
	v_sub_f32_e32 v105, v105, v207
	v_sub_f32_e32 v104, v104, v207
	v_sub_f32_e32 v103, v103, v207
	v_sub_f32_e32 v102, v102, v207
	v_sub_f32_e32 v101, v101, v207
	v_sub_f32_e32 v100, v100, v207
	v_sub_f32_e32 v99, v99, v207
	v_sub_f32_e32 v98, v98, v207
	v_sub_f32_e32 v97, v97, v207
	v_sub_f32_e32 v96, v96, v207
.LBB0_1079:
	v_add_f32_e32 v193, v248, v229
	s_andn2_b64 vcc, exec, s[38:39]
	s_mov_b64 s[40:41], 0
	s_cbranch_vccz .Lslow_in_A

.LBB0_1082:
	s_add_i32 s29, s57, 0x2000
	s_cmpk_lg_i32 s57, 0x4000
	s_cselect_b32 s65, s29, 0
	v_add_co_u32_e32 v2, vcc, 0xeb30000, v14
	v_add_u32_e32 v12, s59, v239
	s_nop 0
	v_addc_co_u32_e32 v3, vcc, 0, v15, vcc
	global_load_dword v192, v[2:3], off
	v_add_co_u32_e32 v2, vcc, 0xeb38000, v14
	s_nop 1
	v_addc_co_u32_e32 v3, vcc, 0, v15, vcc
	global_load_dword v14, v[2:3], off
	global_load_dword v209, v[182:183], off
	v_lshrrev_b32_e32 v2, v238, v0
	v_lshrrev_b32_e32 v3, v238, v190
	v_bfe_u32 v4, v2, 0, 4
	v_lshl_add_u32 v4, v4, 4, s100
	ds_read_b128 v[80:83], v4
	v_bfe_u32 v4, v2, 8, 4
	v_lshl_add_u32 v4, v4, 4, s100
	ds_read_b128 v[84:87], v4
	v_bfe_u32 v4, v2, 16, 4
	v_lshl_add_u32 v4, v4, 4, s100
	ds_read_b128 v[88:91], v4
	v_bfe_u32 v4, v2, 24, 4
	v_lshl_add_u32 v4, v4, 4, s100
	ds_read_b128 v[92:95], v4
	v_bfe_u32 v4, v3, 0, 4
	v_lshl_add_u32 v4, v4, 4, s100
	ds_read_b128 v[96:99], v4
	v_bfe_u32 v4, v3, 8, 4
	v_lshl_add_u32 v4, v4, 4, s100
	ds_read_b128 v[100:103], v4
	v_bfe_u32 v4, v3, 16, 4
	v_lshl_add_u32 v4, v4, 4, s100
	ds_read_b128 v[104:107], v4
	v_bfe_u32 v4, v3, 24, 4
	v_lshl_add_u32 v4, v4, 4, s100
	ds_read_b128 v[108:111], v4
	ds_read_b64_tr_b16 v[156:157], v12 offset:24576
	ds_read_b64_tr_b16 v[158:159], v12 offset:25088
	s_waitcnt lgkmcnt(6)
	v_mfma_f32_32x32x16_bf16 v[80:95], v[140:143], v[124:127], v[80:95]
	ds_read_b64_tr_b16 v[152:153], v12 offset:28672
	ds_read_b64_tr_b16 v[154:155], v12 offset:29184
	s_waitcnt lgkmcnt(4)
	v_mfma_f32_32x32x16_bf16 v[96:111], v[136:139], v[124:127], v[96:111]
	ds_read_b64_tr_b16 v[144:145], v12 offset:25600
	ds_read_b64_tr_b16 v[146:147], v12 offset:26112
	s_waitcnt lgkmcnt(11)
	v_mfma_f32_32x32x16_bf16 v[80:95], v[148:151], v[120:123], v[80:95]
	ds_read_b64_tr_b16 v[148:149], v12 offset:29696
	ds_read_b64_tr_b16 v[150:151], v12 offset:30208
	s_waitcnt lgkmcnt(12)
	v_mfma_f32_32x32x16_bf16 v[96:111], v[176:179], v[120:123], v[96:111]
	ds_read_b64_tr_b16 v[176:177], v12 offset:26624
	ds_read_b64_tr_b16 v[178:179], v12 offset:27136
	s_waitcnt lgkmcnt(13)
	v_mfma_f32_32x32x16_bf16 v[80:95], v[172:175], v[116:119], v[80:95]
	ds_read_b64_tr_b16 v[2:3], v12 offset:30720
	ds_read_b64_tr_b16 v[4:5], v12 offset:31232
	s_waitcnt lgkmcnt(14)
	v_mfma_f32_32x32x16_bf16 v[96:111], v[164:167], v[116:119], v[96:111]
	ds_read_b64_tr_b16 v[6:7], v12 offset:27648
	ds_read_b64_tr_b16 v[8:9], v12 offset:28160
	s_waitcnt lgkmcnt(14)
	v_mfma_f32_32x32x16_bf16 v[80:95], v[168:171], v[112:115], v[80:95]
	ds_read_b64_tr_b16 v[10:11], v12 offset:31744
	ds_read_b64_tr_b16 v[12:13], v12 offset:32256
	v_mfma_f32_32x32x16_bf16 v[96:111], v[160:163], v[112:115], v[96:111]
	v_add_f32_e32 v229, v64, v65
	v_add_f32_e32 v229, v66, v229
	v_add_f32_e32 v229, v67, v229
	v_add_f32_e32 v229, v68, v229
	v_add_f32_e32 v229, v69, v229
	v_add_f32_e32 v229, v70, v229
	v_add_f32_e32 v229, v71, v229
	v_add_f32_e32 v229, v72, v229
	v_add_f32_e32 v229, v73, v229
	v_add_f32_e32 v229, v74, v229
	v_add_f32_e32 v229, v75, v229
	v_add_f32_e32 v229, v76, v229
	v_add_f32_e32 v229, v77, v229
	v_add_f32_e32 v229, v78, v229
	v_add_f32_e32 v229, v79, v229
	v_add_f32_e32 v229, v48, v229
	v_add_f32_e32 v229, v49, v229
	v_add_f32_e32 v229, v50, v229
	v_add_f32_e32 v229, v51, v229
	v_add_f32_e32 v229, v52, v229
	v_add_f32_e32 v229, v53, v229
	v_add_f32_e32 v229, v54, v229
	v_add_f32_e32 v229, v55, v229
	v_add_f32_e32 v229, v56, v229
	v_add_f32_e32 v229, v57, v229
	v_add_f32_e32 v229, v58, v229
	v_add_f32_e32 v229, v59, v229
	v_add_f32_e32 v229, v60, v229
	v_add_f32_e32 v229, v61, v229
	v_add_f32_e32 v229, v62, v229
	v_add_f32_e32 v229, v63, v229
	v_cvt_pk_bf16_f32 v140, v64, v65
	v_cvt_pk_bf16_f32 v141, v66, v67
	v_cvt_pk_bf16_f32 v142, v68, v69
	v_cvt_pk_bf16_f32 v143, v70, v71
	v_cvt_pk_bf16_f32 v136, v72, v73
	v_cvt_pk_bf16_f32 v137, v74, v75
	v_cvt_pk_bf16_f32 v138, v76, v77
	v_cvt_pk_bf16_f32 v139, v78, v79
	v_cvt_pk_bf16_f32 v132, v48, v49
	v_cvt_pk_bf16_f32 v133, v50, v51
	v_cvt_pk_bf16_f32 v134, v52, v53
	v_cvt_pk_bf16_f32 v135, v54, v55
	v_cvt_pk_bf16_f32 v128, v56, v57
	v_cvt_pk_bf16_f32 v129, v58, v59
	v_cvt_pk_bf16_f32 v130, v60, v61
	v_cvt_pk_bf16_f32 v131, v62, v63
	v_lshl_add_u64 v[48:49], v[186:187], 0, s[22:23]
	s_add_i32 s29, s57, s63
	s_mov_b32 m0, s29
	s_nop 0
	global_load_lds_dwordx4 v[48:49], off
	v_lshl_add_u64 v[48:49], v[188:189], 0, s[70:71]
	s_add_i32 s29, s65, s62
	s_mov_b32 m0, s29
	s_nop 0
	global_load_lds_dwordx4 v[48:49], off
	s_waitcnt vmcnt(7)
	v_mul_f32_e32 v48, v201, v191
	v_cmp_nge_f32_e32 vcc, s73, v48
	v_cmp_neq_f32_e64 s[38:39], 0, v207
	s_or_b64 vcc, vcc, s[38:39]
	s_cmp_lg_u64 vcc, 0
	s_cselect_b64 s[38:39], -1, 0
	s_cbranch_vccz .LBB0_1084
	v_sub_f32_e32 v95, v95, v207
	v_sub_f32_e32 v94, v94, v207
	v_sub_f32_e32 v93, v93, v207
	v_sub_f32_e32 v92, v92, v207
	v_sub_f32_e32 v91, v91, v207
	v_sub_f32_e32 v90, v90, v207
	v_sub_f32_e32 v89, v89, v207
	v_sub_f32_e32 v88, v88, v207
	v_sub_f32_e32 v87, v87, v207
	v_sub_f32_e32 v86, v86, v207
	v_sub_f32_e32 v85, v85, v207
	v_sub_f32_e32 v84, v84, v207
	v_sub_f32_e32 v83, v83, v207
	v_sub_f32_e32 v82, v82, v207
	v_sub_f32_e32 v81, v81, v207
	v_sub_f32_e32 v80, v80, v207
	v_sub_f32_e32 v111, v111, v207
	v_sub_f32_e32 v110, v110, v207
	v_sub_f32_e32 v109, v109, v207
	v_sub_f32_e32 v108, v108, v207
	v_sub_f32_e32 v107, v107, v207
	v_sub_f32_e32 v106, v106, v207
	v_sub_f32_e32 v105, v105, v207
	v_sub_f32_e32 v104, v104, v207
	v_sub_f32_e32 v103, v103, v207
	v_sub_f32_e32 v102, v102, v207
	v_sub_f32_e32 v101, v101, v207
	v_sub_f32_e32 v100, v100, v207
	v_sub_f32_e32 v99, v99, v207
	v_sub_f32_e32 v98, v98, v207
	v_sub_f32_e32 v97, v97, v207
	v_sub_f32_e32 v96, v96, v207
.LBB0_1084:
	v_add_f32_e32 v248, v193, v229
	v_or_b32_e32 v15, v213, v211
	v_cmp_ne_u32_e32 vcc, 0, v15
	s_nop 3
	s_or_b64 s[42:43], s[42:43], vcc
	s_andn2_b64 vcc, exec, s[38:39]
	s_mov_b64 s[40:41], 0
	s_cbranch_vccz .Lslow_in_B
